# P8: H2 row write-out rewritten (batched loads, permlane32-widened dwordx4 stores instead of 32 serialized load-wait-store steps)
# speedup vs baseline: 1.0259x; 1.0052x over previous
; __device__ __forceinline__ void p8_route(Frame& F) {
;     ...
;         if (h == 0) ssq[w * 32 + i] = ss;
; #pragma unroll
;         for (int r_ = 0; r_ < 16; ++r_) part[(w * 32 + (r_ & 3) + 8 * (r_ >> 2) + 4 * h) * 33 + i] = acc[r_];
;         __syncthreads();
; #pragma unroll
;         for (int k2 = 0; k2 < 2; ++k2) { const int idx = tid + NTHR * k2, ii = idx >> 5, e = idx & 31; float sm = 0.f, sq = 0.f;
; #pragma unroll
;             for (int ww = 0; ww < 8; ++ww) { sm += part[(ww * 32 + ii) * 33 + e]; sq += ssq[ww * 32 + ii]; }
;             const float rs = 1.f / sqrtf(sq * (1.f / D) + NORM_EPS); lgt[ii * 33 + e] = sm * rs + rtb[e]; if (e == 0) srs[ii] = rs; }
;         __syncthreads();
.LBB0_1430:
	s_or_b64 exec, exec, s[10:11]
	s_nop 6
	ds_write2_b32 v54, v2, v3 offset1:33
	ds_write2_b32 v54, v4, v5 offset0:66 offset1:99
	v_add_u32_e32 v2, 0x400, v54
	ds_write2_b32 v2, v6, v7 offset0:8 offset1:41
	ds_write2_b32 v2, v8, v9 offset0:74 offset1:107
	v_add_u32_e32 v2, 0x800, v54
	ds_write2_b32 v2, v10, v11 offset0:16 offset1:49
	ds_write2_b32 v2, v12, v13 offset0:82 offset1:115
	v_add_u32_e32 v2, 0xc00, v54
	ds_write2_b32 v2, v14, v15 offset0:24 offset1:57
	ds_write2_b32 v2, v16, v17 offset0:90 offset1:123
	s_waitcnt lgkmcnt(0)
	s_barrier
	global_load_dword v2, v[20:21], off
	v_add_u32_e32 v3, 0x8400, v51
	ds_read2_b32 v[4:5], v3 offset1:32
	ds_read_b32 v6, v55
	ds_read_b32 v8, v55 offset:4224
	ds_read_b32 v10, v55 offset:8448
	ds_read_b32 v11, v55 offset:12672
	ds_read_b32 v12, v55 offset:16896
	ds_read_b32 v13, v55 offset:21120
	ds_read_b32 v14, v55 offset:25344
	ds_read_b32 v15, v55 offset:29568
	s_waitcnt lgkmcnt(7)
	v_add_f32_e32 v9, 0, v6
	ds_read2_b32 v[6:7], v3 offset0:64 offset1:96
	s_waitcnt lgkmcnt(7)
	v_add_f32_e32 v16, v9, v8
	ds_read2_b32 v[8:9], v3 offset0:128 offset1:160
	v_add_f32_e32 v4, 0, v4
	v_add_f32_e32 v17, v4, v5
	ds_read2_b32 v[4:5], v3 offset0:192 offset1:224
	s_waitcnt lgkmcnt(2)
	v_add_f32_e32 v3, v17, v6
	v_add_f32_e32 v3, v3, v7
	s_waitcnt lgkmcnt(1)
	v_add_f32_e32 v3, v3, v8
	v_add_f32_e32 v3, v3, v9
	s_waitcnt lgkmcnt(0)
	v_add_f32_e32 v3, v3, v4
	v_add_f32_e32 v3, v3, v5
	v_fmamk_f32 v3, v3, 0x3a000000, v56
	v_mul_f32_e32 v4, 0x4f800000, v3
	v_cmp_gt_f32_e32 vcc, s27, v3
	v_add_f32_e32 v5, v16, v10
	v_add_f32_e32 v5, v5, v11
	v_cndmask_b32_e32 v3, v3, v4, vcc
	v_sqrt_f32_e32 v4, v3
	v_add_f32_e32 v5, v5, v12
	v_add_f32_e32 v5, v5, v13
	v_add_f32_e32 v5, v5, v14
	v_add_u32_e32 v6, -1, v4
	v_fma_f32 v7, -v6, v4, v3
	v_cmp_ge_f32_e64 s[10:11], 0, v7
	v_add_u32_e32 v7, 1, v4
	v_add_f32_e32 v5, v5, v15
	v_cndmask_b32_e64 v6, v4, v6, s[10:11]
	v_fma_f32 v4, -v7, v4, v3
	v_cmp_lt_f32_e64 s[10:11], 0, v4
	s_nop 1
	v_cndmask_b32_e64 v4, v6, v7, s[10:11]
	v_mul_f32_e32 v6, 0x37800000, v4
	v_cndmask_b32_e32 v4, v4, v6, vcc
	v_cmp_class_f32_e32 vcc, v3, v57
	s_nop 1
	v_cndmask_b32_e32 v3, v4, v3, vcc
	v_div_scale_f32 v4, s[10:11], v3, v3, 1.0
	v_rcp_f32_e32 v6, v4
	s_nop 0
	v_fma_f32 v7, -v4, v6, 1.0
	v_fmac_f32_e32 v6, v7, v6
	v_div_scale_f32 v7, vcc, 1.0, v3, 1.0
	v_mul_f32_e32 v8, v7, v6
	v_fma_f32 v9, -v4, v8, v7
	v_fmac_f32_e32 v8, v9, v6
	v_fma_f32 v4, -v4, v8, v7
	v_div_fmas_f32 v4, v4, v6, v8
	v_div_fixup_f32 v3, v4, v3, 1.0
	s_waitcnt vmcnt(0)
	v_fma_f32 v4, v5, v3, v2
	ds_write_b32 v55, v4 offset:34816
	s_and_saveexec_b64 s[10:11], s[6:7]
	ds_write_b32 v51, v3 offset:39040
	s_or_b64 exec, exec, s[10:11]
	v_add_u32_e32 v3, 0x8400, v52
	ds_read2_b32 v[4:5], v3 offset1:32
	ds_read_b32 v6, v58
	ds_read_b32 v8, v58 offset:4224
	ds_read_b32 v10, v58 offset:8448
	ds_read_b32 v11, v58 offset:12672
	ds_read_b32 v12, v58 offset:16896
	ds_read_b32 v13, v58 offset:21120
	ds_read_b32 v14, v58 offset:25344
	ds_read_b32 v15, v58 offset:29568
	s_waitcnt lgkmcnt(7)
	v_add_f32_e32 v9, 0, v6
	ds_read2_b32 v[6:7], v3 offset0:64 offset1:96
	s_waitcnt lgkmcnt(7)
	v_add_f32_e32 v16, v9, v8
	ds_read2_b32 v[8:9], v3 offset0:128 offset1:160
	v_add_f32_e32 v4, 0, v4
	v_add_f32_e32 v17, v4, v5
	ds_read2_b32 v[4:5], v3 offset0:192 offset1:224
	s_waitcnt lgkmcnt(2)
	v_add_f32_e32 v3, v17, v6
	v_add_f32_e32 v3, v3, v7
	s_waitcnt lgkmcnt(1)
	v_add_f32_e32 v3, v3, v8
	v_add_f32_e32 v3, v3, v9
	s_waitcnt lgkmcnt(0)
	v_add_f32_e32 v3, v3, v4
	v_add_f32_e32 v3, v3, v5
	v_fmamk_f32 v3, v3, 0x3a000000, v56
	v_mul_f32_e32 v4, 0x4f800000, v3
	v_cmp_gt_f32_e32 vcc, s27, v3
	v_add_f32_e32 v5, v16, v10
	v_add_f32_e32 v5, v5, v11
	v_cndmask_b32_e32 v3, v3, v4, vcc
	v_sqrt_f32_e32 v4, v3
	v_add_f32_e32 v5, v5, v12
	v_add_f32_e32 v5, v5, v13
	v_add_f32_e32 v5, v5, v14
	v_add_u32_e32 v6, -1, v4
	v_fma_f32 v7, -v6, v4, v3
	v_cmp_ge_f32_e64 s[10:11], 0, v7
	v_add_u32_e32 v7, 1, v4
	v_add_f32_e32 v5, v5, v15
	v_cndmask_b32_e64 v6, v4, v6, s[10:11]
	v_fma_f32 v4, -v7, v4, v3
	v_cmp_lt_f32_e64 s[10:11], 0, v4
	s_nop 1
	v_cndmask_b32_e64 v4, v6, v7, s[10:11]
	v_mul_f32_e32 v6, 0x37800000, v4
	v_cndmask_b32_e32 v4, v4, v6, vcc
	v_cmp_class_f32_e32 vcc, v3, v57
	s_nop 1
	v_cndmask_b32_e32 v3, v4, v3, vcc
	v_div_scale_f32 v4, s[10:11], v3, v3, 1.0
	v_rcp_f32_e32 v6, v4
	s_nop 0
	v_fma_f32 v7, -v4, v6, 1.0
	v_fmac_f32_e32 v6, v7, v6
	v_div_scale_f32 v7, vcc, 1.0, v3, 1.0
	v_mul_f32_e32 v8, v7, v6
	v_fma_f32 v9, -v4, v8, v7
	v_fmac_f32_e32 v8, v9, v6
	v_fma_f32 v4, -v4, v8, v7
	v_div_fmas_f32 v4, v4, v6, v8
	v_div_fixup_f32 v3, v4, v3, 1.0
	v_fmac_f32_e32 v2, v5, v3
	ds_write_b32 v58, v2 offset:34816
	s_and_saveexec_b64 s[10:11], s[6:7]
	ds_write_b32 v52, v3 offset:39040
	s_or_b64 exec, exec, s[10:11]
	s_waitcnt lgkmcnt(0)
	s_barrier
; __device__ __forceinline__ unsigned pk4f8(float a, float b, float c, float d) { int r = 0; r = __builtin_amdgcn_cvt_pk_fp8_f32(a, b, r, false); r = __builtin_amdgcn_cvt_pk_fp8_f32(c, d, r, true); return (unsigned)r; }
; #define UNP4(v) ((f32x4){__uint_as_float((v).x << 16), __uint_as_float((v).x & 0xffff0000u), __uint_as_float((v).y << 16), __uint_as_float((v).y & 0xffff0000u)})
; __device__ __forceinline__ void p8_route(Frame& F) {
;     ...
;         { const float rs = srs[i] * F8_SX; unsigned char* orow = H2 + (size_t)(m0 + i) * D + 256 * w + 4 * h;
; #pragma unroll 8
;           for (int q = 0; q < 32; ++q) { const f32x4 n4 = *(const f32x4*)(nw + 256 * w + 4 * h + 8 * q); const v2u xb_ = *(const v2u*)(xrow + 8 * q); const f32x4 hv = UNP4(xb_) * rs * n4; *(unsigned*)(orow + 8 * q) = pk4f8(hv[0], hv[1], hv[2], hv[3]); } }
	ds_read_b32 v6, v50 offset:39040
	v_lshlrev_b64 v[2:3], 11, v[28:29]
	v_lshl_add_u64 v[2:3], v[30:31], 0, v[2:3]
	v_lshl_add_u64 v[4:5], v[32:33], 0, v[34:35]
	s_mov_b64 s[10:11], 0
	s_waitcnt lgkmcnt(0)
	v_mul_f32_e32 v6, 0x41000000, v6
	v_mov_b32_e32 v7, v6
	v_mov_b32_e32 v8, v6
	v_mov_b32_e32 v9, v6
	global_load_dwordx2 v[76:77], v[4:5], off offset:-64
	global_load_dwordx2 v[78:79], v[4:5], off offset:-48
	global_load_dwordx2 v[80:81], v[4:5], off offset:-32
	global_load_dwordx2 v[82:83], v[4:5], off offset:-16
	global_load_dwordx2 v[84:85], v[4:5], off offset:0
	global_load_dwordx2 v[86:87], v[4:5], off offset:16
	global_load_dwordx2 v[88:89], v[4:5], off offset:32
	global_load_dwordx2 v[90:91], v[4:5], off offset:48
	global_load_dwordx2 v[92:93], v[4:5], off offset:64
	global_load_dwordx2 v[94:95], v[4:5], off offset:80
	global_load_dwordx2 v[96:97], v[4:5], off offset:96
	global_load_dwordx2 v[98:99], v[4:5], off offset:112
	global_load_dwordx2 v[100:101], v[4:5], off offset:128
	global_load_dwordx2 v[102:103], v[4:5], off offset:144
	global_load_dwordx2 v[104:105], v[4:5], off offset:160
	global_load_dwordx2 v[106:107], v[4:5], off offset:176
	global_load_dwordx2 v[108:109], v[4:5], off offset:192
	global_load_dwordx2 v[110:111], v[4:5], off offset:208
	global_load_dwordx2 v[112:113], v[4:5], off offset:224
	global_load_dwordx2 v[114:115], v[4:5], off offset:240
	global_load_dwordx2 v[116:117], v[4:5], off offset:256
	global_load_dwordx2 v[118:119], v[4:5], off offset:272
	global_load_dwordx2 v[120:121], v[4:5], off offset:288
	global_load_dwordx2 v[122:123], v[4:5], off offset:304
	global_load_dwordx2 v[124:125], v[4:5], off offset:320
	global_load_dwordx2 v[126:127], v[4:5], off offset:336
	global_load_dwordx2 v[128:129], v[4:5], off offset:352
	global_load_dwordx2 v[130:131], v[4:5], off offset:368
	global_load_dwordx2 v[132:133], v[4:5], off offset:384
	global_load_dwordx2 v[134:135], v[4:5], off offset:400
	global_load_dwordx2 v[136:137], v[4:5], off offset:416
	global_load_dwordx2 v[138:139], v[4:5], off offset:432
	global_load_dwordx4 v[140:143], v[22:23], off offset:0
	global_load_dwordx4 v[144:147], v[22:23], off offset:32
	global_load_dwordx4 v[148:151], v[22:23], off offset:64
	global_load_dwordx4 v[152:155], v[22:23], off offset:96
	global_load_dwordx4 v[156:159], v[22:23], off offset:128
	global_load_dwordx4 v[164:167], v[22:23], off offset:160
	global_load_dwordx4 v[168:171], v[22:23], off offset:192
	global_load_dwordx4 v[172:175], v[22:23], off offset:224
	global_load_dwordx4 v[180:183], v[22:23], off offset:256
	global_load_dwordx4 v[184:187], v[22:23], off offset:288
	global_load_dwordx4 v[188:191], v[22:23], off offset:320
	global_load_dwordx4 v[192:195], v[22:23], off offset:352
	global_load_dwordx4 v[196:199], v[22:23], off offset:384
	global_load_dwordx4 v[200:203], v[22:23], off offset:416
	global_load_dwordx4 v[204:207], v[22:23], off offset:448
	global_load_dwordx4 v[208:211], v[22:23], off offset:480
	v_lshrrev_b32_e32 v34, 5, v162
	v_mul_u32_u24_e32 v34, 12, v34
	v_mov_b32_e32 v35, 0
	v_lshl_add_u64 v[2:3], v[2:3], 0, v[34:35]
	s_waitcnt vmcnt(0)
	v_lshlrev_b32_e32 v10, 16, v76
	v_lshlrev_b32_e32 v14, 16, v78
	v_lshlrev_b32_e32 v36, 16, v80
	v_lshlrev_b32_e32 v40, 16, v82
	v_and_b32_e32 v11, 0xffff0000, v76
	v_and_b32_e32 v15, 0xffff0000, v78
	v_and_b32_e32 v37, 0xffff0000, v80
	v_and_b32_e32 v41, 0xffff0000, v82
	v_lshlrev_b32_e32 v12, 16, v77
	v_lshlrev_b32_e32 v16, 16, v79
	v_lshlrev_b32_e32 v38, 16, v81
	v_lshlrev_b32_e32 v42, 16, v83
	v_and_b32_e32 v13, 0xffff0000, v77
	v_and_b32_e32 v17, 0xffff0000, v79
	v_and_b32_e32 v39, 0xffff0000, v81
	v_and_b32_e32 v43, 0xffff0000, v83
	v_pk_mul_f32 v[10:11], v[6:7], v[10:11]
	v_pk_mul_f32 v[14:15], v[6:7], v[14:15]
	v_pk_mul_f32 v[36:37], v[6:7], v[36:37]
	v_pk_mul_f32 v[40:41], v[6:7], v[40:41]
	v_pk_mul_f32 v[12:13], v[8:9], v[12:13]
	v_pk_mul_f32 v[16:17], v[8:9], v[16:17]
	v_pk_mul_f32 v[38:39], v[8:9], v[38:39]
	v_pk_mul_f32 v[42:43], v[8:9], v[42:43]
	v_pk_mul_f32 v[140:141], v[140:141], v[10:11]
	v_pk_mul_f32 v[144:145], v[144:145], v[14:15]
	v_pk_mul_f32 v[148:149], v[148:149], v[36:37]
	v_pk_mul_f32 v[152:153], v[152:153], v[40:41]
	v_pk_mul_f32 v[142:143], v[142:143], v[12:13]
	v_pk_mul_f32 v[146:147], v[146:147], v[16:17]
	v_pk_mul_f32 v[150:151], v[150:151], v[38:39]
	v_pk_mul_f32 v[154:155], v[154:155], v[42:43]
	v_cvt_pk_fp8_f32 v212, v140, v141
	v_cvt_pk_fp8_f32 v214, v144, v145
	v_cvt_pk_fp8_f32 v213, v148, v149
	v_cvt_pk_fp8_f32 v215, v152, v153
	v_cvt_pk_fp8_f32 v212, v142, v143 op_sel:[0,0,1]
	v_cvt_pk_fp8_f32 v214, v146, v147 op_sel:[0,0,1]
	v_cvt_pk_fp8_f32 v213, v150, v151 op_sel:[0,0,1]
	v_cvt_pk_fp8_f32 v215, v154, v155 op_sel:[0,0,1]
	v_lshlrev_b32_e32 v10, 16, v84
	v_lshlrev_b32_e32 v14, 16, v86
	v_lshlrev_b32_e32 v36, 16, v88
	v_lshlrev_b32_e32 v40, 16, v90
	v_and_b32_e32 v11, 0xffff0000, v84
	v_and_b32_e32 v15, 0xffff0000, v86
	v_and_b32_e32 v37, 0xffff0000, v88
	v_and_b32_e32 v41, 0xffff0000, v90
	v_lshlrev_b32_e32 v12, 16, v85
	v_lshlrev_b32_e32 v16, 16, v87
	v_lshlrev_b32_e32 v38, 16, v89
	v_lshlrev_b32_e32 v42, 16, v91
	v_and_b32_e32 v13, 0xffff0000, v85
	v_and_b32_e32 v17, 0xffff0000, v87
	v_and_b32_e32 v39, 0xffff0000, v89
	v_and_b32_e32 v43, 0xffff0000, v91
	v_pk_mul_f32 v[10:11], v[6:7], v[10:11]
	v_pk_mul_f32 v[14:15], v[6:7], v[14:15]
	v_pk_mul_f32 v[36:37], v[6:7], v[36:37]
	v_pk_mul_f32 v[40:41], v[6:7], v[40:41]
	v_pk_mul_f32 v[12:13], v[8:9], v[12:13]
	v_pk_mul_f32 v[16:17], v[8:9], v[16:17]
	v_pk_mul_f32 v[38:39], v[8:9], v[38:39]
	v_pk_mul_f32 v[42:43], v[8:9], v[42:43]
	v_pk_mul_f32 v[156:157], v[156:157], v[10:11]
; __device__ __forceinline__ unsigned pk4f8(float a, float b, float c, float d) { int r = 0; r = __builtin_amdgcn_cvt_pk_fp8_f32(a, b, r, false); r = __builtin_amdgcn_cvt_pk_fp8_f32(c, d, r, true); return (unsigned)r; }
; #define UNP4(v) ((f32x4){__uint_as_float((v).x << 16), __uint_as_float((v).x & 0xffff0000u), __uint_as_float((v).y << 16), __uint_as_float((v).y & 0xffff0000u)})
; __device__ __forceinline__ void p8_route(Frame& F) {
;     ...
;         { const float rs = srs[i] * F8_SX; unsigned char* orow = H2 + (size_t)(m0 + i) * D + 256 * w + 4 * h;
; #pragma unroll 8
;           for (int q = 0; q < 32; ++q) { const f32x4 n4 = *(const f32x4*)(nw + 256 * w + 4 * h + 8 * q); const v2u xb_ = *(const v2u*)(xrow + 8 * q); const f32x4 hv = UNP4(xb_) * rs * n4; *(unsigned*)(orow + 8 * q) = pk4f8(hv[0], hv[1], hv[2], hv[3]); } }
	v_pk_mul_f32 v[164:165], v[164:165], v[14:15]
	v_pk_mul_f32 v[168:169], v[168:169], v[36:37]
	v_pk_mul_f32 v[172:173], v[172:173], v[40:41]
	v_pk_mul_f32 v[158:159], v[158:159], v[12:13]
	v_pk_mul_f32 v[166:167], v[166:167], v[16:17]
	v_pk_mul_f32 v[170:171], v[170:171], v[38:39]
	v_pk_mul_f32 v[174:175], v[174:175], v[42:43]
	v_cvt_pk_fp8_f32 v216, v156, v157
	v_cvt_pk_fp8_f32 v218, v164, v165
	v_cvt_pk_fp8_f32 v217, v168, v169
	v_cvt_pk_fp8_f32 v219, v172, v173
	v_cvt_pk_fp8_f32 v216, v158, v159 op_sel:[0,0,1]
	v_cvt_pk_fp8_f32 v218, v166, v167 op_sel:[0,0,1]
	v_cvt_pk_fp8_f32 v217, v170, v171 op_sel:[0,0,1]
	v_cvt_pk_fp8_f32 v219, v174, v175 op_sel:[0,0,1]
	v_lshlrev_b32_e32 v10, 16, v92
	v_lshlrev_b32_e32 v14, 16, v94
	v_lshlrev_b32_e32 v36, 16, v96
	v_lshlrev_b32_e32 v40, 16, v98
	v_and_b32_e32 v11, 0xffff0000, v92
	v_and_b32_e32 v15, 0xffff0000, v94
	v_and_b32_e32 v37, 0xffff0000, v96
	v_and_b32_e32 v41, 0xffff0000, v98
	v_lshlrev_b32_e32 v12, 16, v93
	v_lshlrev_b32_e32 v16, 16, v95
	v_lshlrev_b32_e32 v38, 16, v97
	v_lshlrev_b32_e32 v42, 16, v99
	v_and_b32_e32 v13, 0xffff0000, v93
	v_and_b32_e32 v17, 0xffff0000, v95
	v_and_b32_e32 v39, 0xffff0000, v97
	v_and_b32_e32 v43, 0xffff0000, v99
	v_pk_mul_f32 v[10:11], v[6:7], v[10:11]
	v_pk_mul_f32 v[14:15], v[6:7], v[14:15]
	v_pk_mul_f32 v[36:37], v[6:7], v[36:37]
	v_pk_mul_f32 v[40:41], v[6:7], v[40:41]
	v_pk_mul_f32 v[12:13], v[8:9], v[12:13]
	v_pk_mul_f32 v[16:17], v[8:9], v[16:17]
	v_pk_mul_f32 v[38:39], v[8:9], v[38:39]
	v_pk_mul_f32 v[42:43], v[8:9], v[42:43]
	v_pk_mul_f32 v[180:181], v[180:181], v[10:11]
	v_pk_mul_f32 v[184:185], v[184:185], v[14:15]
	v_pk_mul_f32 v[188:189], v[188:189], v[36:37]
	v_pk_mul_f32 v[192:193], v[192:193], v[40:41]
	v_pk_mul_f32 v[182:183], v[182:183], v[12:13]
	v_pk_mul_f32 v[186:187], v[186:187], v[16:17]
	v_pk_mul_f32 v[190:191], v[190:191], v[38:39]
	v_pk_mul_f32 v[194:195], v[194:195], v[42:43]
	v_cvt_pk_fp8_f32 v220, v180, v181
	v_cvt_pk_fp8_f32 v222, v184, v185
	v_cvt_pk_fp8_f32 v221, v188, v189
	v_cvt_pk_fp8_f32 v223, v192, v193
	v_cvt_pk_fp8_f32 v220, v182, v183 op_sel:[0,0,1]
	v_cvt_pk_fp8_f32 v222, v186, v187 op_sel:[0,0,1]
	v_cvt_pk_fp8_f32 v221, v190, v191 op_sel:[0,0,1]
	v_cvt_pk_fp8_f32 v223, v194, v195 op_sel:[0,0,1]
	v_lshlrev_b32_e32 v10, 16, v100
	v_lshlrev_b32_e32 v14, 16, v102
	v_lshlrev_b32_e32 v36, 16, v104
	v_lshlrev_b32_e32 v40, 16, v106
	v_and_b32_e32 v11, 0xffff0000, v100
	v_and_b32_e32 v15, 0xffff0000, v102
	v_and_b32_e32 v37, 0xffff0000, v104
	v_and_b32_e32 v41, 0xffff0000, v106
	v_lshlrev_b32_e32 v12, 16, v101
	v_lshlrev_b32_e32 v16, 16, v103
	v_lshlrev_b32_e32 v38, 16, v105
	v_lshlrev_b32_e32 v42, 16, v107
	v_and_b32_e32 v13, 0xffff0000, v101
	v_and_b32_e32 v17, 0xffff0000, v103
	v_and_b32_e32 v39, 0xffff0000, v105
	v_and_b32_e32 v43, 0xffff0000, v107
	v_pk_mul_f32 v[10:11], v[6:7], v[10:11]
	v_pk_mul_f32 v[14:15], v[6:7], v[14:15]
	v_pk_mul_f32 v[36:37], v[6:7], v[36:37]
	v_pk_mul_f32 v[40:41], v[6:7], v[40:41]
	v_pk_mul_f32 v[12:13], v[8:9], v[12:13]
	v_pk_mul_f32 v[16:17], v[8:9], v[16:17]
	v_pk_mul_f32 v[38:39], v[8:9], v[38:39]
	v_pk_mul_f32 v[42:43], v[8:9], v[42:43]
	v_pk_mul_f32 v[196:197], v[196:197], v[10:11]
	v_pk_mul_f32 v[200:201], v[200:201], v[14:15]
	v_pk_mul_f32 v[204:205], v[204:205], v[36:37]
	v_pk_mul_f32 v[208:209], v[208:209], v[40:41]
	v_pk_mul_f32 v[198:199], v[198:199], v[12:13]
	v_pk_mul_f32 v[202:203], v[202:203], v[16:17]
	v_pk_mul_f32 v[206:207], v[206:207], v[38:39]
	v_pk_mul_f32 v[210:211], v[210:211], v[42:43]
	v_cvt_pk_fp8_f32 v224, v196, v197
	v_cvt_pk_fp8_f32 v226, v200, v201
	v_cvt_pk_fp8_f32 v225, v204, v205
	v_cvt_pk_fp8_f32 v227, v208, v209
	v_cvt_pk_fp8_f32 v224, v198, v199 op_sel:[0,0,1]
	v_cvt_pk_fp8_f32 v226, v202, v203 op_sel:[0,0,1]
	v_cvt_pk_fp8_f32 v225, v206, v207 op_sel:[0,0,1]
	v_cvt_pk_fp8_f32 v227, v210, v211 op_sel:[0,0,1]
	s_nop 1
	global_load_dwordx4 v[140:143], v[22:23], off offset:512
	global_load_dwordx4 v[144:147], v[22:23], off offset:544
	global_load_dwordx4 v[148:151], v[22:23], off offset:576
	global_load_dwordx4 v[152:155], v[22:23], off offset:608
	global_load_dwordx4 v[156:159], v[22:23], off offset:640
	global_load_dwordx4 v[164:167], v[22:23], off offset:672
	global_load_dwordx4 v[168:171], v[22:23], off offset:704
	global_load_dwordx4 v[172:175], v[22:23], off offset:736
	global_load_dwordx4 v[180:183], v[22:23], off offset:768
	global_load_dwordx4 v[184:187], v[22:23], off offset:800
	global_load_dwordx4 v[188:191], v[22:23], off offset:832
	global_load_dwordx4 v[192:195], v[22:23], off offset:864
	global_load_dwordx4 v[196:199], v[22:23], off offset:896
	global_load_dwordx4 v[200:203], v[22:23], off offset:928
	global_load_dwordx4 v[204:207], v[22:23], off offset:960
	global_load_dwordx4 v[208:211], v[22:23], off offset:992
	v_permlane32_swap_b32 v212, v213
	v_permlane32_swap_b32 v214, v215
	global_store_dwordx4 v[2:3], v[212:215], off offset:-32
	v_permlane32_swap_b32 v216, v217
	v_permlane32_swap_b32 v218, v219
	global_store_dwordx4 v[2:3], v[216:219], off offset:0
	v_permlane32_swap_b32 v220, v221
	v_permlane32_swap_b32 v222, v223
	global_store_dwordx4 v[2:3], v[220:223], off offset:32
	v_permlane32_swap_b32 v224, v225
	v_permlane32_swap_b32 v226, v227
	global_store_dwordx4 v[2:3], v[224:227], off offset:64
	s_waitcnt vmcnt(0)
; #define LAS __attribute__((address_space(3)))
; __device__ __forceinline__ unsigned pk4f8(float a, float b, float c, float d) { int r = 0; r = __builtin_amdgcn_cvt_pk_fp8_f32(a, b, r, false); r = __builtin_amdgcn_cvt_pk_fp8_f32(c, d, r, true); return (unsigned)r; }
; #define UNP4(v) ((f32x4){__uint_as_float((v).x << 16), __uint_as_float((v).x & 0xffff0000u), __uint_as_float((v).y << 16), __uint_as_float((v).y & 0xffff0000u)})
; __device__ __forceinline__ void p8_route(Frame& F) {
;     ...
;         { const float rs = srs[i] * F8_SX; unsigned char* orow = H2 + (size_t)(m0 + i) * D + 256 * w + 4 * h;
; #pragma unroll 8
;           for (int q = 0; q < 32; ++q) { const f32x4 n4 = *(const f32x4*)(nw + 256 * w + 4 * h + 8 * q); const v2u xb_ = *(const v2u*)(xrow + 8 * q); const f32x4 hv = UNP4(xb_) * rs * n4; *(unsigned*)(orow + 8 * q) = pk4f8(hv[0], hv[1], hv[2], hv[3]); } }
;         if (tid < 32) { const LAS float* lr = lgt + tid * 33; unsigned used = 0u; int idx[4]; float val[4];
	v_lshlrev_b32_e32 v10, 16, v108
	v_lshlrev_b32_e32 v14, 16, v110
	v_lshlrev_b32_e32 v36, 16, v112
	v_lshlrev_b32_e32 v40, 16, v114
	v_and_b32_e32 v11, 0xffff0000, v108
	v_and_b32_e32 v15, 0xffff0000, v110
	v_and_b32_e32 v37, 0xffff0000, v112
	v_and_b32_e32 v41, 0xffff0000, v114
	v_lshlrev_b32_e32 v12, 16, v109
	v_lshlrev_b32_e32 v16, 16, v111
	v_lshlrev_b32_e32 v38, 16, v113
	v_lshlrev_b32_e32 v42, 16, v115
	v_and_b32_e32 v13, 0xffff0000, v109
	v_and_b32_e32 v17, 0xffff0000, v111
	v_and_b32_e32 v39, 0xffff0000, v113
	v_and_b32_e32 v43, 0xffff0000, v115
	v_pk_mul_f32 v[10:11], v[6:7], v[10:11]
	v_pk_mul_f32 v[14:15], v[6:7], v[14:15]
	v_pk_mul_f32 v[36:37], v[6:7], v[36:37]
	v_pk_mul_f32 v[40:41], v[6:7], v[40:41]
	v_pk_mul_f32 v[12:13], v[8:9], v[12:13]
	v_pk_mul_f32 v[16:17], v[8:9], v[16:17]
	v_pk_mul_f32 v[38:39], v[8:9], v[38:39]
	v_pk_mul_f32 v[42:43], v[8:9], v[42:43]
	v_pk_mul_f32 v[140:141], v[140:141], v[10:11]
	v_pk_mul_f32 v[144:145], v[144:145], v[14:15]
	v_pk_mul_f32 v[148:149], v[148:149], v[36:37]
	v_pk_mul_f32 v[152:153], v[152:153], v[40:41]
	v_pk_mul_f32 v[142:143], v[142:143], v[12:13]
	v_pk_mul_f32 v[146:147], v[146:147], v[16:17]
	v_pk_mul_f32 v[150:151], v[150:151], v[38:39]
	v_pk_mul_f32 v[154:155], v[154:155], v[42:43]
	v_cvt_pk_fp8_f32 v228, v140, v141
	v_cvt_pk_fp8_f32 v230, v144, v145
	v_cvt_pk_fp8_f32 v229, v148, v149
	v_cvt_pk_fp8_f32 v231, v152, v153
	v_cvt_pk_fp8_f32 v228, v142, v143 op_sel:[0,0,1]
	v_cvt_pk_fp8_f32 v230, v146, v147 op_sel:[0,0,1]
	v_cvt_pk_fp8_f32 v229, v150, v151 op_sel:[0,0,1]
	v_cvt_pk_fp8_f32 v231, v154, v155 op_sel:[0,0,1]
	v_lshlrev_b32_e32 v10, 16, v116
	v_lshlrev_b32_e32 v14, 16, v118
	v_lshlrev_b32_e32 v36, 16, v120
	v_lshlrev_b32_e32 v40, 16, v122
	v_and_b32_e32 v11, 0xffff0000, v116
	v_and_b32_e32 v15, 0xffff0000, v118
	v_and_b32_e32 v37, 0xffff0000, v120
	v_and_b32_e32 v41, 0xffff0000, v122
	v_lshlrev_b32_e32 v12, 16, v117
	v_lshlrev_b32_e32 v16, 16, v119
	v_lshlrev_b32_e32 v38, 16, v121
	v_lshlrev_b32_e32 v42, 16, v123
	v_and_b32_e32 v13, 0xffff0000, v117
	v_and_b32_e32 v17, 0xffff0000, v119
	v_and_b32_e32 v39, 0xffff0000, v121
	v_and_b32_e32 v43, 0xffff0000, v123
	v_pk_mul_f32 v[10:11], v[6:7], v[10:11]
	v_pk_mul_f32 v[14:15], v[6:7], v[14:15]
	v_pk_mul_f32 v[36:37], v[6:7], v[36:37]
	v_pk_mul_f32 v[40:41], v[6:7], v[40:41]
	v_pk_mul_f32 v[12:13], v[8:9], v[12:13]
	v_pk_mul_f32 v[16:17], v[8:9], v[16:17]
	v_pk_mul_f32 v[38:39], v[8:9], v[38:39]
	v_pk_mul_f32 v[42:43], v[8:9], v[42:43]
	v_pk_mul_f32 v[156:157], v[156:157], v[10:11]
	v_pk_mul_f32 v[164:165], v[164:165], v[14:15]
	v_pk_mul_f32 v[168:169], v[168:169], v[36:37]
	v_pk_mul_f32 v[172:173], v[172:173], v[40:41]
	v_pk_mul_f32 v[158:159], v[158:159], v[12:13]
	v_pk_mul_f32 v[166:167], v[166:167], v[16:17]
	v_pk_mul_f32 v[170:171], v[170:171], v[38:39]
	v_pk_mul_f32 v[174:175], v[174:175], v[42:43]
	v_cvt_pk_fp8_f32 v232, v156, v157
	v_cvt_pk_fp8_f32 v234, v164, v165
	v_cvt_pk_fp8_f32 v233, v168, v169
	v_cvt_pk_fp8_f32 v235, v172, v173
	v_cvt_pk_fp8_f32 v232, v158, v159 op_sel:[0,0,1]
	v_cvt_pk_fp8_f32 v234, v166, v167 op_sel:[0,0,1]
	v_cvt_pk_fp8_f32 v233, v170, v171 op_sel:[0,0,1]
	v_cvt_pk_fp8_f32 v235, v174, v175 op_sel:[0,0,1]
	v_lshlrev_b32_e32 v10, 16, v124
	v_lshlrev_b32_e32 v14, 16, v126
	v_lshlrev_b32_e32 v36, 16, v128
	v_lshlrev_b32_e32 v40, 16, v130
	v_and_b32_e32 v11, 0xffff0000, v124
	v_and_b32_e32 v15, 0xffff0000, v126
	v_and_b32_e32 v37, 0xffff0000, v128
	v_and_b32_e32 v41, 0xffff0000, v130
	v_lshlrev_b32_e32 v12, 16, v125
	v_lshlrev_b32_e32 v16, 16, v127
	v_lshlrev_b32_e32 v38, 16, v129
	v_lshlrev_b32_e32 v42, 16, v131
	v_and_b32_e32 v13, 0xffff0000, v125
	v_and_b32_e32 v17, 0xffff0000, v127
	v_and_b32_e32 v39, 0xffff0000, v129
	v_and_b32_e32 v43, 0xffff0000, v131
	v_pk_mul_f32 v[10:11], v[6:7], v[10:11]
	v_pk_mul_f32 v[14:15], v[6:7], v[14:15]
	v_pk_mul_f32 v[36:37], v[6:7], v[36:37]
	v_pk_mul_f32 v[40:41], v[6:7], v[40:41]
	v_pk_mul_f32 v[12:13], v[8:9], v[12:13]
	v_pk_mul_f32 v[16:17], v[8:9], v[16:17]
	v_pk_mul_f32 v[38:39], v[8:9], v[38:39]
	v_pk_mul_f32 v[42:43], v[8:9], v[42:43]
	v_pk_mul_f32 v[180:181], v[180:181], v[10:11]
	v_pk_mul_f32 v[184:185], v[184:185], v[14:15]
	v_pk_mul_f32 v[188:189], v[188:189], v[36:37]
	v_pk_mul_f32 v[192:193], v[192:193], v[40:41]
	v_pk_mul_f32 v[182:183], v[182:183], v[12:13]
	v_pk_mul_f32 v[186:187], v[186:187], v[16:17]
	v_pk_mul_f32 v[190:191], v[190:191], v[38:39]
	v_pk_mul_f32 v[194:195], v[194:195], v[42:43]
	v_cvt_pk_fp8_f32 v64, v180, v181
	v_cvt_pk_fp8_f32 v66, v184, v185
	v_cvt_pk_fp8_f32 v65, v188, v189
	v_cvt_pk_fp8_f32 v67, v192, v193
	v_cvt_pk_fp8_f32 v64, v182, v183 op_sel:[0,0,1]
	v_cvt_pk_fp8_f32 v66, v186, v187 op_sel:[0,0,1]
	v_cvt_pk_fp8_f32 v65, v190, v191 op_sel:[0,0,1]
	v_cvt_pk_fp8_f32 v67, v194, v195 op_sel:[0,0,1]
	v_lshlrev_b32_e32 v10, 16, v132
	v_lshlrev_b32_e32 v14, 16, v134
	v_lshlrev_b32_e32 v36, 16, v136
	v_lshlrev_b32_e32 v40, 16, v138
	v_and_b32_e32 v11, 0xffff0000, v132
	v_and_b32_e32 v15, 0xffff0000, v134
	v_and_b32_e32 v37, 0xffff0000, v136
	v_and_b32_e32 v41, 0xffff0000, v138
	v_lshlrev_b32_e32 v12, 16, v133
	v_lshlrev_b32_e32 v16, 16, v135
	v_lshlrev_b32_e32 v38, 16, v137
	v_lshlrev_b32_e32 v42, 16, v139
	v_and_b32_e32 v13, 0xffff0000, v133
	v_and_b32_e32 v17, 0xffff0000, v135
	v_and_b32_e32 v39, 0xffff0000, v137
	v_and_b32_e32 v43, 0xffff0000, v139
	v_pk_mul_f32 v[10:11], v[6:7], v[10:11]
	v_pk_mul_f32 v[14:15], v[6:7], v[14:15]
	v_pk_mul_f32 v[36:37], v[6:7], v[36:37]
	v_pk_mul_f32 v[40:41], v[6:7], v[40:41]
	v_pk_mul_f32 v[12:13], v[8:9], v[12:13]
	v_pk_mul_f32 v[16:17], v[8:9], v[16:17]
	v_pk_mul_f32 v[38:39], v[8:9], v[38:39]
	v_pk_mul_f32 v[42:43], v[8:9], v[42:43]
	v_pk_mul_f32 v[196:197], v[196:197], v[10:11]
	v_pk_mul_f32 v[200:201], v[200:201], v[14:15]
	v_pk_mul_f32 v[204:205], v[204:205], v[36:37]
	v_pk_mul_f32 v[208:209], v[208:209], v[40:41]
	v_pk_mul_f32 v[198:199], v[198:199], v[12:13]
	v_pk_mul_f32 v[202:203], v[202:203], v[16:17]
	v_pk_mul_f32 v[206:207], v[206:207], v[38:39]
	v_pk_mul_f32 v[210:211], v[210:211], v[42:43]
	v_cvt_pk_fp8_f32 v68, v196, v197
	v_cvt_pk_fp8_f32 v70, v200, v201
	v_cvt_pk_fp8_f32 v69, v204, v205
	v_cvt_pk_fp8_f32 v71, v208, v209
	v_cvt_pk_fp8_f32 v68, v198, v199 op_sel:[0,0,1]
	v_cvt_pk_fp8_f32 v70, v202, v203 op_sel:[0,0,1]
	v_cvt_pk_fp8_f32 v69, v206, v207 op_sel:[0,0,1]
	v_cvt_pk_fp8_f32 v71, v210, v211 op_sel:[0,0,1]
	s_nop 1
	v_permlane32_swap_b32 v228, v229
	v_permlane32_swap_b32 v230, v231
	global_store_dwordx4 v[2:3], v[228:231], off offset:96
	v_permlane32_swap_b32 v232, v233
	v_permlane32_swap_b32 v234, v235
	global_store_dwordx4 v[2:3], v[232:235], off offset:128
	v_permlane32_swap_b32 v64, v65
	v_permlane32_swap_b32 v66, v67
	global_store_dwordx4 v[2:3], v[64:67], off offset:160
	v_permlane32_swap_b32 v68, v69
	v_permlane32_swap_b32 v70, v71
	global_store_dwordx4 v[2:3], v[68:71], off offset:192
	s_and_saveexec_b64 s[22:23], s[8:9]
	s_cbranch_execz .LBB0_1425
; #define LAS __attribute__((address_space(3)))
; __device__ __forceinline__ void p8_route(Frame& F) {
;     ...
;         if (tid < 32) { const LAS float* lr = lgt + tid * 33; unsigned used = 0u; int idx[4]; float val[4];
; #pragma unroll
;             for (int s4 = 0; s4 < 4; ++s4) { float best = -INFINITY; int bi = 0;
;                 for (int e = 0; e < 32; ++e) { const float v = lr[e]; const bool ok = !((used >> e) & 1u) && (v > best); best = ok ? v : best; bi = ok ? e : bi; }
;                 used |= 1u << bi; idx[s4] = bi; val[s4] = best; }
	v_add_u32_e32 v2, 0x8800, v59
	ds_read2_b32 v[10:11], v2 offset1:1
	v_add_u32_e32 v2, 0x8808, v59
	v_add_u32_e32 v4, 0x8818, v59
	v_add_u32_e32 v3, 0x8810, v59
	ds_read2_b32 v[40:41], v2 offset1:1
	ds_read2_b32 v[12:13], v3 offset1:1
	ds_read2_b32 v[4:5], v4 offset1:1
	s_waitcnt lgkmcnt(3)
	v_max_f32_e32 v2, v10, v10
	v_max_f32_e32 v2, 0xff800000, v2
	v_cmp_gt_f32_e32 vcc, v11, v2
	v_add_u32_e32 v6, 0x8820, v59
	ds_read2_b32 v[14:15], v6 offset1:1
	v_cndmask_b32_e32 v2, v2, v11, vcc
	v_cndmask_b32_e64 v3, 0, 1, vcc
	s_waitcnt lgkmcnt(3)
	v_cmp_gt_f32_e32 vcc, v40, v2
	v_add_u32_e32 v6, 0x8828, v59
	v_add_u32_e32 v7, 0x8830, v59
	v_cndmask_b32_e32 v2, v2, v40, vcc
	v_cndmask_b32_e64 v3, v3, 2, vcc
	v_cmp_gt_f32_e32 vcc, v41, v2
	v_add_u32_e32 v8, 0x8838, v59
	ds_read2_b32 v[44:45], v6 offset1:1
	ds_read2_b32 v[16:17], v7 offset1:1
	ds_read2_b32 v[6:7], v8 offset1:1
	v_cndmask_b32_e32 v2, v2, v41, vcc
	v_cndmask_b32_e64 v3, v3, 3, vcc
	s_waitcnt lgkmcnt(5)
	v_cmp_gt_f32_e32 vcc, v12, v2
	v_add_u32_e32 v8, 0x8840, v59
	ds_read2_b32 v[34:35], v8 offset1:1
	v_cndmask_b32_e32 v2, v2, v12, vcc
	v_cndmask_b32_e64 v3, v3, 4, vcc
	v_cmp_gt_f32_e32 vcc, v13, v2
	v_add_u32_e32 v8, 0x8848, v59
	v_add_u32_e32 v9, 0x8850, v59
	v_cndmask_b32_e32 v2, v2, v13, vcc
	v_cndmask_b32_e64 v3, v3, 5, vcc
	s_waitcnt lgkmcnt(5)
	v_cmp_gt_f32_e32 vcc, v4, v2
	v_add_u32_e32 v18, 0x8858, v59
	ds_read2_b32 v[46:47], v8 offset1:1
	ds_read2_b32 v[36:37], v9 offset1:1
	ds_read2_b32 v[8:9], v18 offset1:1
	v_cndmask_b32_e32 v2, v2, v4, vcc
	v_cndmask_b32_e64 v3, v3, 6, vcc
	v_cmp_gt_f32_e32 vcc, v5, v2
	v_add_u32_e32 v62, 0x8878, v59
	s_nop 0
	v_cndmask_b32_e32 v2, v2, v5, vcc
	v_cndmask_b32_e64 v3, v3, 7, vcc
	s_waitcnt lgkmcnt(7)
	v_cmp_gt_f32_e32 vcc, v14, v2
	s_nop 1
	v_cndmask_b32_e32 v2, v2, v14, vcc
	v_cndmask_b32_e64 v3, v3, 8, vcc
	v_cmp_gt_f32_e32 vcc, v15, v2
	s_nop 1
	v_cndmask_b32_e32 v2, v2, v15, vcc
	v_cndmask_b32_e64 v3, v3, 9, vcc
	s_waitcnt lgkmcnt(6)
	v_cmp_gt_f32_e32 vcc, v44, v2
	s_nop 1
	v_cndmask_b32_e32 v2, v2, v44, vcc
	v_cndmask_b32_e64 v3, v3, 10, vcc
	v_cmp_gt_f32_e32 vcc, v45, v2
	s_nop 1
	v_cndmask_b32_e32 v2, v2, v45, vcc
	v_cndmask_b32_e64 v3, v3, 11, vcc
	s_waitcnt lgkmcnt(5)
	v_cmp_gt_f32_e32 vcc, v16, v2
	s_nop 1
	v_cndmask_b32_e32 v2, v2, v16, vcc
	v_cndmask_b32_e64 v3, v3, 12, vcc
	v_cmp_gt_f32_e32 vcc, v17, v2
	s_nop 1
	v_cndmask_b32_e32 v2, v2, v17, vcc
	v_cndmask_b32_e64 v3, v3, 13, vcc
	s_waitcnt lgkmcnt(4)
	v_cmp_gt_f32_e32 vcc, v6, v2
	s_nop 1
	v_cndmask_b32_e32 v2, v2, v6, vcc
	v_cndmask_b32_e64 v3, v3, 14, vcc
	v_cmp_gt_f32_e32 vcc, v7, v2
	s_nop 1
	v_cndmask_b32_e32 v2, v2, v7, vcc
	v_cndmask_b32_e64 v3, v3, 15, vcc
	s_waitcnt lgkmcnt(3)
	v_cmp_gt_f32_e32 vcc, v34, v2
	s_nop 1
	v_cndmask_b32_e32 v2, v2, v34, vcc
	v_cndmask_b32_e64 v3, v3, 16, vcc
	v_cmp_gt_f32_e32 vcc, v35, v2
	s_nop 1
	v_cndmask_b32_e32 v2, v2, v35, vcc
	v_cndmask_b32_e64 v3, v3, 17, vcc
	s_waitcnt lgkmcnt(2)
	v_cmp_gt_f32_e32 vcc, v46, v2
	s_nop 1
	v_cndmask_b32_e32 v2, v2, v46, vcc
	v_cndmask_b32_e64 v3, v3, 18, vcc
	v_cmp_gt_f32_e32 vcc, v47, v2
	s_nop 1
	v_cndmask_b32_e32 v2, v2, v47, vcc
	v_cndmask_b32_e64 v3, v3, 19, vcc
	s_waitcnt lgkmcnt(1)
	v_cmp_gt_f32_e32 vcc, v36, v2
	s_nop 1
	v_cndmask_b32_e32 v2, v2, v36, vcc
	v_cndmask_b32_e64 v3, v3, 20, vcc
	v_cmp_gt_f32_e32 vcc, v37, v2
	s_nop 1
	v_cndmask_b32_e32 v2, v2, v37, vcc
	v_cndmask_b32_e64 v3, v3, 21, vcc
	s_waitcnt lgkmcnt(0)
	v_cmp_gt_f32_e32 vcc, v8, v2
	s_nop 1
	v_cndmask_b32_e32 v2, v2, v8, vcc
	v_cndmask_b32_e64 v3, v3, 22, vcc
	v_cmp_gt_f32_e32 vcc, v9, v2
	s_nop 1
	v_cndmask_b32_e32 v18, v2, v9, vcc
	v_add_u32_e32 v2, 0x8860, v59
	ds_read2_b32 v[38:39], v2 offset1:1
	v_cndmask_b32_e64 v29, v3, 23, vcc
	v_add_u32_e32 v2, 0x8868, v59
	v_add_u32_e32 v3, 0x8870, v59
	ds_read2_b32 v[48:49], v2 offset1:1
	ds_read2_b32 v[42:43], v3 offset1:1
	ds_read2_b32 v[2:3], v62 offset1:1
	s_waitcnt lgkmcnt(3)
	v_cmp_gt_f32_e32 vcc, v38, v18
	s_nop 1
	v_cndmask_b32_e32 v18, v18, v38, vcc
	v_cndmask_b32_e64 v29, v29, 24, vcc
	v_cmp_gt_f32_e32 vcc, v39, v18
	s_nop 1
	v_cndmask_b32_e32 v18, v18, v39, vcc
	v_cndmask_b32_e64 v29, v29, 25, vcc
	s_waitcnt lgkmcnt(2)
	v_cmp_gt_f32_e32 vcc, v48, v18
	s_nop 1
	v_cndmask_b32_e32 v18, v18, v48, vcc
	v_cndmask_b32_e64 v29, v29, 26, vcc
	v_cmp_gt_f32_e32 vcc, v49, v18
	s_nop 1
	v_cndmask_b32_e32 v18, v18, v49, vcc
	v_cndmask_b32_e64 v29, v29, 27, vcc
	s_waitcnt lgkmcnt(1)
	v_cmp_gt_f32_e32 vcc, v42, v18
	s_nop 1
	v_cndmask_b32_e32 v18, v18, v42, vcc
	v_cndmask_b32_e64 v29, v29, 28, vcc
	v_cmp_gt_f32_e32 vcc, v43, v18
	s_nop 1
	v_cndmask_b32_e32 v18, v18, v43, vcc
	v_cndmask_b32_e64 v29, v29, 29, vcc
	s_waitcnt lgkmcnt(0)
; __device__ __forceinline__ void p8_route(Frame& F) {
;     ...
;             for (int s4 = 0; s4 < 4; ++s4) { float best = -INFINITY; int bi = 0;
;                 for (int e = 0; e < 32; ++e) { const float v = lr[e]; const bool ok = !((used >> e) & 1u) && (v > best); best = ok ? v : best; bi = ok ? e : bi; }
;                 used |= 1u << bi; idx[s4] = bi; val[s4] = best; }
	v_cmp_gt_f32_e32 vcc, v2, v18
	s_nop 1
	v_cndmask_b32_e32 v18, v18, v2, vcc
	v_cndmask_b32_e64 v29, v29, 30, vcc
	v_cmp_gt_f32_e32 vcc, v3, v18
	s_nop 1
	v_cndmask_b32_e64 v29, v29, 31, vcc
	v_cndmask_b32_e32 v62, v18, v3, vcc
	v_cmp_ne_u32_e64 s[10:11], 0, v29
	v_cmp_lg_f32_e32 vcc, s29, v10
	v_lshlrev_b32_e64 v18, v29, 1
	s_and_b64 s[10:11], s[10:11], vcc
	v_cndmask_b32_e64 v63, v61, v10, s[10:11]
	v_and_b32_e32 v64, 2, v18
	v_cmp_eq_u32_e64 s[10:11], 0, v64
	v_cmp_gt_f32_e64 s[12:13], v11, v63
	s_and_b64 s[10:11], s[10:11], s[12:13]
	v_cndmask_b32_e64 v63, v63, v11, s[10:11]
	v_and_b32_e32 v65, 4, v18
	v_cndmask_b32_e64 v64, 0, 1, s[10:11]
	v_cmp_eq_u32_e64 s[10:11], 0, v65
	v_cmp_gt_f32_e64 s[12:13], v40, v63
	s_and_b64 s[10:11], s[10:11], s[12:13]
	v_cndmask_b32_e64 v63, v63, v40, s[10:11]
	v_and_b32_e32 v65, 8, v18
	v_cndmask_b32_e64 v64, v64, 2, s[10:11]
	v_cmp_eq_u32_e64 s[10:11], 0, v65
	v_cmp_gt_f32_e64 s[12:13], v41, v63
	s_and_b64 s[10:11], s[10:11], s[12:13]
	v_cndmask_b32_e64 v63, v63, v41, s[10:11]
	v_and_b32_e32 v65, 16, v18
	v_cndmask_b32_e64 v64, v64, 3, s[10:11]
	v_cmp_eq_u32_e64 s[10:11], 0, v65
	v_cmp_gt_f32_e64 s[12:13], v12, v63
	s_and_b64 s[10:11], s[10:11], s[12:13]
	v_cndmask_b32_e64 v63, v63, v12, s[10:11]
	v_and_b32_e32 v65, 32, v18
	v_cndmask_b32_e64 v64, v64, 4, s[10:11]
	v_cmp_eq_u32_e64 s[10:11], 0, v65
	v_cmp_gt_f32_e64 s[12:13], v13, v63
	s_and_b64 s[10:11], s[10:11], s[12:13]
	v_cndmask_b32_e64 v63, v63, v13, s[10:11]
	v_and_b32_e32 v65, 64, v18
	v_cndmask_b32_e64 v64, v64, 5, s[10:11]
	v_cmp_eq_u32_e64 s[10:11], 0, v65
	v_cmp_gt_f32_e64 s[12:13], v4, v63
	s_and_b64 s[10:11], s[10:11], s[12:13]
	v_cndmask_b32_e64 v63, v63, v4, s[10:11]
	v_and_b32_e32 v65, 0x80, v18
	v_cndmask_b32_e64 v64, v64, 6, s[10:11]
	v_cmp_eq_u32_e64 s[10:11], 0, v65
	v_cmp_gt_f32_e64 s[12:13], v5, v63
	s_and_b64 s[10:11], s[10:11], s[12:13]
	v_cndmask_b32_e64 v63, v63, v5, s[10:11]
	v_and_b32_e32 v65, 0x100, v18
	v_cndmask_b32_e64 v64, v64, 7, s[10:11]
	v_cmp_eq_u32_e64 s[10:11], 0, v65
	v_cmp_gt_f32_e64 s[12:13], v14, v63
	s_and_b64 s[10:11], s[10:11], s[12:13]
	v_cndmask_b32_e64 v63, v63, v14, s[10:11]
	v_and_b32_e32 v65, 0x200, v18
	v_cndmask_b32_e64 v64, v64, 8, s[10:11]
	v_cmp_eq_u32_e64 s[10:11], 0, v65
	v_cmp_gt_f32_e64 s[12:13], v15, v63
	s_and_b64 s[10:11], s[10:11], s[12:13]
	v_cndmask_b32_e64 v63, v63, v15, s[10:11]
	v_and_b32_e32 v65, 0x400, v18
	v_cndmask_b32_e64 v64, v64, 9, s[10:11]
	v_cmp_eq_u32_e64 s[10:11], 0, v65
	v_cmp_gt_f32_e64 s[12:13], v44, v63
	s_and_b64 s[10:11], s[10:11], s[12:13]
	v_cndmask_b32_e64 v63, v63, v44, s[10:11]
	v_and_b32_e32 v65, 0x800, v18
	v_cndmask_b32_e64 v64, v64, 10, s[10:11]
	v_cmp_eq_u32_e64 s[10:11], 0, v65
	v_cmp_gt_f32_e64 s[12:13], v45, v63
	s_and_b64 s[10:11], s[10:11], s[12:13]
	v_cndmask_b32_e64 v63, v63, v45, s[10:11]
	v_and_b32_e32 v65, 0x1000, v18
	v_cndmask_b32_e64 v64, v64, 11, s[10:11]
	v_cmp_eq_u32_e64 s[10:11], 0, v65
	v_cmp_gt_f32_e64 s[12:13], v16, v63
	s_and_b64 s[10:11], s[10:11], s[12:13]
	v_cndmask_b32_e64 v63, v63, v16, s[10:11]
	v_and_b32_e32 v65, 0x2000, v18
	v_cndmask_b32_e64 v64, v64, 12, s[10:11]
	v_cmp_eq_u32_e64 s[10:11], 0, v65
	v_cmp_gt_f32_e64 s[12:13], v17, v63
	s_and_b64 s[10:11], s[10:11], s[12:13]
	v_cndmask_b32_e64 v63, v63, v17, s[10:11]
	v_and_b32_e32 v65, 0x4000, v18
	v_cndmask_b32_e64 v64, v64, 13, s[10:11]
	v_cmp_eq_u32_e64 s[10:11], 0, v65
	v_cmp_gt_f32_e64 s[12:13], v6, v63
	s_and_b64 s[10:11], s[10:11], s[12:13]
	v_cndmask_b32_e64 v63, v63, v6, s[10:11]
	v_and_b32_e32 v65, 0x8000, v18
	v_cndmask_b32_e64 v64, v64, 14, s[10:11]
	v_cmp_eq_u32_e64 s[10:11], 0, v65
	v_cmp_gt_f32_e64 s[12:13], v7, v63
	s_and_b64 s[10:11], s[10:11], s[12:13]
	v_cndmask_b32_e64 v63, v63, v7, s[10:11]
	v_and_b32_e32 v65, 0x10000, v18
	v_cndmask_b32_e64 v64, v64, 15, s[10:11]
	v_cmp_eq_u32_e64 s[10:11], 0, v65
	v_cmp_gt_f32_e64 s[12:13], v34, v63
	s_and_b64 s[10:11], s[10:11], s[12:13]
	v_cndmask_b32_e64 v63, v63, v34, s[10:11]
	v_and_b32_e32 v65, 0x20000, v18
	v_cndmask_b32_e64 v64, v64, 16, s[10:11]
	v_cmp_eq_u32_e64 s[10:11], 0, v65
	v_cmp_gt_f32_e64 s[12:13], v35, v63
	s_and_b64 s[10:11], s[10:11], s[12:13]
	v_cndmask_b32_e64 v63, v63, v35, s[10:11]
	v_and_b32_e32 v65, 0x40000, v18
	v_cndmask_b32_e64 v64, v64, 17, s[10:11]
	v_cmp_eq_u32_e64 s[10:11], 0, v65
	v_cmp_gt_f32_e64 s[12:13], v46, v63
	s_and_b64 s[10:11], s[10:11], s[12:13]
	v_cndmask_b32_e64 v63, v63, v46, s[10:11]
	v_and_b32_e32 v65, 0x80000, v18
	v_cndmask_b32_e64 v64, v64, 18, s[10:11]
	v_cmp_eq_u32_e64 s[10:11], 0, v65
	v_cmp_gt_f32_e64 s[12:13], v47, v63
	s_and_b64 s[10:11], s[10:11], s[12:13]
	v_cndmask_b32_e64 v63, v63, v47, s[10:11]
	v_and_b32_e32 v65, 0x100000, v18
	v_cndmask_b32_e64 v64, v64, 19, s[10:11]
	v_cmp_eq_u32_e64 s[10:11], 0, v65
	v_cmp_gt_f32_e64 s[12:13], v36, v63
	s_and_b64 s[10:11], s[10:11], s[12:13]
	v_cndmask_b32_e64 v63, v63, v36, s[10:11]
	v_and_b32_e32 v65, 0x200000, v18
	v_cndmask_b32_e64 v64, v64, 20, s[10:11]
	v_cmp_eq_u32_e64 s[10:11], 0, v65
	v_cmp_gt_f32_e64 s[12:13], v37, v63
	s_and_b64 s[10:11], s[10:11], s[12:13]
	v_cndmask_b32_e64 v63, v63, v37, s[10:11]
	v_and_b32_e32 v65, 0x400000, v18
	v_cndmask_b32_e64 v64, v64, 21, s[10:11]
	v_cmp_eq_u32_e64 s[10:11], 0, v65
	v_cmp_gt_f32_e64 s[12:13], v8, v63
	s_and_b64 s[10:11], s[10:11], s[12:13]
	v_cndmask_b32_e64 v63, v63, v8, s[10:11]
	v_and_b32_e32 v65, 0x800000, v18
	v_cndmask_b32_e64 v64, v64, 22, s[10:11]
	v_cmp_eq_u32_e64 s[10:11], 0, v65
	v_cmp_gt_f32_e64 s[12:13], v9, v63
	s_and_b64 s[10:11], s[10:11], s[12:13]
	v_cndmask_b32_e64 v63, v63, v9, s[10:11]
	v_and_b32_e32 v65, 0x1000000, v18
; __device__ __forceinline__ void p8_route(Frame& F) {
;     ...
;             for (int s4 = 0; s4 < 4; ++s4) { float best = -INFINITY; int bi = 0;
;                 for (int e = 0; e < 32; ++e) { const float v = lr[e]; const bool ok = !((used >> e) & 1u) && (v > best); best = ok ? v : best; bi = ok ? e : bi; }
;                 used |= 1u << bi; idx[s4] = bi; val[s4] = best; }
	v_cndmask_b32_e64 v64, v64, 23, s[10:11]
	v_cmp_eq_u32_e64 s[10:11], 0, v65
	v_cmp_gt_f32_e64 s[12:13], v38, v63
	s_and_b64 s[10:11], s[10:11], s[12:13]
	v_cndmask_b32_e64 v63, v63, v38, s[10:11]
	v_and_b32_e32 v65, 0x2000000, v18
	v_cndmask_b32_e64 v64, v64, 24, s[10:11]
	v_cmp_eq_u32_e64 s[10:11], 0, v65
	v_cmp_gt_f32_e64 s[12:13], v39, v63
	s_and_b64 s[10:11], s[10:11], s[12:13]
	v_cndmask_b32_e64 v63, v63, v39, s[10:11]
	v_and_b32_e32 v65, 0x4000000, v18
	v_cndmask_b32_e64 v64, v64, 25, s[10:11]
	v_cmp_eq_u32_e64 s[10:11], 0, v65
	v_cmp_gt_f32_e64 s[12:13], v48, v63
	s_and_b64 s[10:11], s[10:11], s[12:13]
	v_cndmask_b32_e64 v63, v63, v48, s[10:11]
	v_and_b32_e32 v65, 0x8000000, v18
	v_cndmask_b32_e64 v64, v64, 26, s[10:11]
	v_cmp_eq_u32_e64 s[10:11], 0, v65
	v_cmp_gt_f32_e64 s[12:13], v49, v63
	s_and_b64 s[10:11], s[10:11], s[12:13]
	v_cndmask_b32_e64 v63, v63, v49, s[10:11]
	v_and_b32_e32 v65, 0x10000000, v18
	v_cndmask_b32_e64 v64, v64, 27, s[10:11]
	v_cmp_eq_u32_e64 s[10:11], 0, v65
	v_cmp_gt_f32_e64 s[12:13], v42, v63
	s_and_b64 s[10:11], s[10:11], s[12:13]
	v_cndmask_b32_e64 v63, v63, v42, s[10:11]
	v_and_b32_e32 v65, 0x20000000, v18
	v_cndmask_b32_e64 v64, v64, 28, s[10:11]
	v_cmp_eq_u32_e64 s[10:11], 0, v65
	v_cmp_gt_f32_e64 s[12:13], v43, v63
	s_and_b64 s[10:11], s[10:11], s[12:13]
	v_cndmask_b32_e64 v63, v63, v43, s[10:11]
	v_and_b32_e32 v65, 2.0, v18
	v_cndmask_b32_e64 v64, v64, 29, s[10:11]
	v_cmp_eq_u32_e64 s[10:11], 0, v65
	v_cmp_gt_f32_e64 s[12:13], v2, v63
	s_and_b64 s[10:11], s[10:11], s[12:13]
	v_cndmask_b32_e64 v63, v63, v2, s[10:11]
	v_cndmask_b32_e64 v64, v64, 30, s[10:11]
	v_cmp_ne_u32_e64 s[10:11], 31, v29
	v_cmp_gt_f32_e64 s[12:13], v3, v63
	s_and_b64 s[10:11], s[10:11], s[12:13]
	v_cndmask_b32_e64 v64, v64, 31, s[10:11]
	v_lshl_or_b32 v65, 1, v64, v18
	v_and_b32_e32 v18, 1, v65
	v_cndmask_b32_e64 v63, v63, v3, s[10:11]
	v_cmp_eq_u32_e64 s[10:11], 0, v18
	s_and_b64 s[10:11], s[10:11], vcc
	v_and_b32_e32 v66, 2, v65
	v_cndmask_b32_e64 v18, v61, v10, s[10:11]
	v_cmp_eq_u32_e64 s[10:11], 0, v66
	v_cmp_gt_f32_e64 s[12:13], v11, v18
	s_and_b64 s[10:11], s[10:11], s[12:13]
	v_cndmask_b32_e64 v18, v18, v11, s[10:11]
	v_and_b32_e32 v67, 4, v65
	v_cndmask_b32_e64 v66, 0, 1, s[10:11]
	v_cmp_eq_u32_e64 s[10:11], 0, v67
	v_cmp_gt_f32_e64 s[12:13], v40, v18
	s_and_b64 s[10:11], s[10:11], s[12:13]
	v_cndmask_b32_e64 v18, v18, v40, s[10:11]
	v_and_b32_e32 v67, 8, v65
	v_cndmask_b32_e64 v66, v66, 2, s[10:11]
	v_cmp_eq_u32_e64 s[10:11], 0, v67
	v_cmp_gt_f32_e64 s[12:13], v41, v18
	s_and_b64 s[10:11], s[10:11], s[12:13]
	v_cndmask_b32_e64 v18, v18, v41, s[10:11]
	v_and_b32_e32 v67, 16, v65
	v_cndmask_b32_e64 v66, v66, 3, s[10:11]
	v_cmp_eq_u32_e64 s[10:11], 0, v67
	v_cmp_gt_f32_e64 s[12:13], v12, v18
	s_and_b64 s[10:11], s[10:11], s[12:13]
	v_cndmask_b32_e64 v18, v18, v12, s[10:11]
	v_and_b32_e32 v67, 32, v65
	v_cndmask_b32_e64 v66, v66, 4, s[10:11]
	v_cmp_eq_u32_e64 s[10:11], 0, v67
	v_cmp_gt_f32_e64 s[12:13], v13, v18
	s_and_b64 s[10:11], s[10:11], s[12:13]
	v_cndmask_b32_e64 v18, v18, v13, s[10:11]
	v_and_b32_e32 v67, 64, v65
	v_cndmask_b32_e64 v66, v66, 5, s[10:11]
	v_cmp_eq_u32_e64 s[10:11], 0, v67
	v_cmp_gt_f32_e64 s[12:13], v4, v18
	s_and_b64 s[10:11], s[10:11], s[12:13]
	v_cndmask_b32_e64 v18, v18, v4, s[10:11]
	v_and_b32_e32 v67, 0x80, v65
	v_cndmask_b32_e64 v66, v66, 6, s[10:11]
	v_cmp_eq_u32_e64 s[10:11], 0, v67
	v_cmp_gt_f32_e64 s[12:13], v5, v18
	s_and_b64 s[10:11], s[10:11], s[12:13]
	v_cndmask_b32_e64 v18, v18, v5, s[10:11]
	v_and_b32_e32 v67, 0x100, v65
	v_cndmask_b32_e64 v66, v66, 7, s[10:11]
	v_cmp_eq_u32_e64 s[10:11], 0, v67
	v_cmp_gt_f32_e64 s[12:13], v14, v18
	s_and_b64 s[10:11], s[10:11], s[12:13]
	v_cndmask_b32_e64 v18, v18, v14, s[10:11]
	v_and_b32_e32 v67, 0x200, v65
	v_cndmask_b32_e64 v66, v66, 8, s[10:11]
	v_cmp_eq_u32_e64 s[10:11], 0, v67
	v_cmp_gt_f32_e64 s[12:13], v15, v18
	s_and_b64 s[10:11], s[10:11], s[12:13]
	v_cndmask_b32_e64 v18, v18, v15, s[10:11]
	v_and_b32_e32 v67, 0x400, v65
	v_cndmask_b32_e64 v66, v66, 9, s[10:11]
	v_cmp_eq_u32_e64 s[10:11], 0, v67
	v_cmp_gt_f32_e64 s[12:13], v44, v18
	s_and_b64 s[10:11], s[10:11], s[12:13]
	v_cndmask_b32_e64 v18, v18, v44, s[10:11]
	v_and_b32_e32 v67, 0x800, v65
	v_cndmask_b32_e64 v66, v66, 10, s[10:11]
	v_cmp_eq_u32_e64 s[10:11], 0, v67
	v_cmp_gt_f32_e64 s[12:13], v45, v18
	s_and_b64 s[10:11], s[10:11], s[12:13]
	v_cndmask_b32_e64 v18, v18, v45, s[10:11]
	v_and_b32_e32 v67, 0x1000, v65
	v_cndmask_b32_e64 v66, v66, 11, s[10:11]
	v_cmp_eq_u32_e64 s[10:11], 0, v67
	v_cmp_gt_f32_e64 s[12:13], v16, v18
	s_and_b64 s[10:11], s[10:11], s[12:13]
	v_cndmask_b32_e64 v18, v18, v16, s[10:11]
	v_and_b32_e32 v67, 0x2000, v65
	v_cndmask_b32_e64 v66, v66, 12, s[10:11]
	v_cmp_eq_u32_e64 s[10:11], 0, v67
	v_cmp_gt_f32_e64 s[12:13], v17, v18
	s_and_b64 s[10:11], s[10:11], s[12:13]
	v_cndmask_b32_e64 v18, v18, v17, s[10:11]
	v_and_b32_e32 v67, 0x4000, v65
	v_cndmask_b32_e64 v66, v66, 13, s[10:11]
	v_cmp_eq_u32_e64 s[10:11], 0, v67
	v_cmp_gt_f32_e64 s[12:13], v6, v18
	s_and_b64 s[10:11], s[10:11], s[12:13]
	v_cndmask_b32_e64 v18, v18, v6, s[10:11]
	v_and_b32_e32 v67, 0x8000, v65
	v_cndmask_b32_e64 v66, v66, 14, s[10:11]
	v_cmp_eq_u32_e64 s[10:11], 0, v67
	v_cmp_gt_f32_e64 s[12:13], v7, v18
	s_and_b64 s[10:11], s[10:11], s[12:13]
	v_cndmask_b32_e64 v18, v18, v7, s[10:11]
	v_and_b32_e32 v67, 0x10000, v65
	v_cndmask_b32_e64 v66, v66, 15, s[10:11]
	v_cmp_eq_u32_e64 s[10:11], 0, v67
	v_cmp_gt_f32_e64 s[12:13], v34, v18
	s_and_b64 s[10:11], s[10:11], s[12:13]
	v_cndmask_b32_e64 v18, v18, v34, s[10:11]
	v_and_b32_e32 v67, 0x20000, v65
	v_cndmask_b32_e64 v66, v66, 16, s[10:11]
; __device__ __forceinline__ void p8_route(Frame& F) {
;     ...
;             for (int s4 = 0; s4 < 4; ++s4) { float best = -INFINITY; int bi = 0;
;                 for (int e = 0; e < 32; ++e) { const float v = lr[e]; const bool ok = !((used >> e) & 1u) && (v > best); best = ok ? v : best; bi = ok ? e : bi; }
;                 used |= 1u << bi; idx[s4] = bi; val[s4] = best; }
	v_cmp_eq_u32_e64 s[10:11], 0, v67
	v_cmp_gt_f32_e64 s[12:13], v35, v18
	s_and_b64 s[10:11], s[10:11], s[12:13]
	v_cndmask_b32_e64 v18, v18, v35, s[10:11]
	v_and_b32_e32 v67, 0x40000, v65
	v_cndmask_b32_e64 v66, v66, 17, s[10:11]
	v_cmp_eq_u32_e64 s[10:11], 0, v67
	v_cmp_gt_f32_e64 s[12:13], v46, v18
	s_and_b64 s[10:11], s[10:11], s[12:13]
	v_cndmask_b32_e64 v18, v18, v46, s[10:11]
	v_and_b32_e32 v67, 0x80000, v65
	v_cndmask_b32_e64 v66, v66, 18, s[10:11]
	v_cmp_eq_u32_e64 s[10:11], 0, v67
	v_cmp_gt_f32_e64 s[12:13], v47, v18
	s_and_b64 s[10:11], s[10:11], s[12:13]
	v_cndmask_b32_e64 v18, v18, v47, s[10:11]
	v_and_b32_e32 v67, 0x100000, v65
	v_cndmask_b32_e64 v66, v66, 19, s[10:11]
	v_cmp_eq_u32_e64 s[10:11], 0, v67
	v_cmp_gt_f32_e64 s[12:13], v36, v18
	s_and_b64 s[10:11], s[10:11], s[12:13]
	v_cndmask_b32_e64 v18, v18, v36, s[10:11]
	v_and_b32_e32 v67, 0x200000, v65
	v_cndmask_b32_e64 v66, v66, 20, s[10:11]
	v_cmp_eq_u32_e64 s[10:11], 0, v67
	v_cmp_gt_f32_e64 s[12:13], v37, v18
	s_and_b64 s[10:11], s[10:11], s[12:13]
	v_cndmask_b32_e64 v18, v18, v37, s[10:11]
	v_and_b32_e32 v67, 0x400000, v65
	v_cndmask_b32_e64 v66, v66, 21, s[10:11]
	v_cmp_eq_u32_e64 s[10:11], 0, v67
	v_cmp_gt_f32_e64 s[12:13], v8, v18
	s_and_b64 s[10:11], s[10:11], s[12:13]
	v_cndmask_b32_e64 v18, v18, v8, s[10:11]
	v_and_b32_e32 v67, 0x800000, v65
	v_cndmask_b32_e64 v66, v66, 22, s[10:11]
	v_cmp_eq_u32_e64 s[10:11], 0, v67
	v_cmp_gt_f32_e64 s[12:13], v9, v18
	s_and_b64 s[10:11], s[10:11], s[12:13]
	v_cndmask_b32_e64 v18, v18, v9, s[10:11]
	v_and_b32_e32 v67, 0x1000000, v65
	v_cndmask_b32_e64 v66, v66, 23, s[10:11]
	v_cmp_eq_u32_e64 s[10:11], 0, v67
	v_cmp_gt_f32_e64 s[12:13], v38, v18
	s_and_b64 s[10:11], s[10:11], s[12:13]
	v_cndmask_b32_e64 v18, v18, v38, s[10:11]
	v_and_b32_e32 v67, 0x2000000, v65
	v_cndmask_b32_e64 v66, v66, 24, s[10:11]
	v_cmp_eq_u32_e64 s[10:11], 0, v67
	v_cmp_gt_f32_e64 s[12:13], v39, v18
	s_and_b64 s[10:11], s[10:11], s[12:13]
	v_cndmask_b32_e64 v18, v18, v39, s[10:11]
	v_and_b32_e32 v67, 0x4000000, v65
	v_cndmask_b32_e64 v66, v66, 25, s[10:11]
	v_cmp_eq_u32_e64 s[10:11], 0, v67
	v_cmp_gt_f32_e64 s[12:13], v48, v18
	s_and_b64 s[10:11], s[10:11], s[12:13]
	v_cndmask_b32_e64 v18, v18, v48, s[10:11]
	v_and_b32_e32 v67, 0x8000000, v65
	v_cndmask_b32_e64 v66, v66, 26, s[10:11]
	v_cmp_eq_u32_e64 s[10:11], 0, v67
	v_cmp_gt_f32_e64 s[12:13], v49, v18
	s_and_b64 s[10:11], s[10:11], s[12:13]
	v_cndmask_b32_e64 v18, v18, v49, s[10:11]
	v_and_b32_e32 v67, 0x10000000, v65
	v_cndmask_b32_e64 v66, v66, 27, s[10:11]
	v_cmp_eq_u32_e64 s[10:11], 0, v67
	v_cmp_gt_f32_e64 s[12:13], v42, v18
	s_and_b64 s[10:11], s[10:11], s[12:13]
	v_cndmask_b32_e64 v18, v18, v42, s[10:11]
	v_and_b32_e32 v67, 0x20000000, v65
	v_cndmask_b32_e64 v66, v66, 28, s[10:11]
	v_cmp_eq_u32_e64 s[10:11], 0, v67
	v_cmp_gt_f32_e64 s[12:13], v43, v18
	s_and_b64 s[10:11], s[10:11], s[12:13]
	v_cndmask_b32_e64 v18, v18, v43, s[10:11]
	v_and_b32_e32 v67, 2.0, v65
	v_cndmask_b32_e64 v66, v66, 29, s[10:11]
	v_cmp_eq_u32_e64 s[10:11], 0, v67
	v_cmp_gt_f32_e64 s[12:13], v2, v18
	s_and_b64 s[10:11], s[10:11], s[12:13]
	v_cndmask_b32_e64 v18, v18, v2, s[10:11]
	v_cndmask_b32_e64 v66, v66, 30, s[10:11]
	v_cmp_lt_i32_e64 s[10:11], -1, v65
	v_cmp_gt_f32_e64 s[12:13], v3, v18
	s_and_b64 s[10:11], s[10:11], s[12:13]
	v_cndmask_b32_e64 v66, v66, 31, s[10:11]
	v_lshlrev_b32_e64 v68, v66, 1
	v_cndmask_b32_e64 v67, v18, v3, s[10:11]
	v_bitop3_b32 v18, v68, 1, v65 bitop3:0xc8
	v_cmp_eq_u32_e64 s[10:11], 0, v18
	s_and_b64 vcc, s[10:11], vcc
	v_cndmask_b32_e32 v10, v61, v10, vcc
	v_bitop3_b32 v18, v68, 2, v65 bitop3:0xc8
	v_cmp_eq_u32_e32 vcc, 0, v18
	v_cmp_gt_f32_e64 s[10:11], v11, v10
	s_and_b64 vcc, vcc, s[10:11]
	v_cndmask_b32_e32 v10, v10, v11, vcc
	v_bitop3_b32 v18, v68, 4, v65 bitop3:0xc8
	v_cndmask_b32_e64 v11, 0, 1, vcc
	v_cmp_eq_u32_e32 vcc, 0, v18
	v_cmp_gt_f32_e64 s[10:11], v40, v10
	s_and_b64 vcc, vcc, s[10:11]
	v_cndmask_b32_e32 v10, v10, v40, vcc
	v_bitop3_b32 v18, v68, 8, v65 bitop3:0xc8
	v_cndmask_b32_e64 v11, v11, 2, vcc
	v_cmp_eq_u32_e32 vcc, 0, v18
	v_cmp_gt_f32_e64 s[10:11], v41, v10
	s_and_b64 vcc, vcc, s[10:11]
	v_cndmask_b32_e32 v10, v10, v41, vcc
	v_bitop3_b32 v18, v68, 16, v65 bitop3:0xc8
	v_cndmask_b32_e64 v11, v11, 3, vcc
	v_cmp_eq_u32_e32 vcc, 0, v18
	v_cmp_gt_f32_e64 s[10:11], v12, v10
	s_and_b64 vcc, vcc, s[10:11]
	v_cndmask_b32_e32 v10, v10, v12, vcc
	v_bitop3_b32 v12, v68, 32, v65 bitop3:0xc8
	v_cndmask_b32_e64 v11, v11, 4, vcc
	v_cmp_eq_u32_e32 vcc, 0, v12
	v_cmp_gt_f32_e64 s[10:11], v13, v10
	s_and_b64 vcc, vcc, s[10:11]
	v_cndmask_b32_e32 v10, v10, v13, vcc
	v_bitop3_b32 v12, v68, 64, v65 bitop3:0xc8
	v_cndmask_b32_e64 v11, v11, 5, vcc
	v_cmp_eq_u32_e32 vcc, 0, v12
	v_cmp_gt_f32_e64 s[10:11], v4, v10
	s_and_b64 vcc, vcc, s[10:11]
	v_cndmask_b32_e32 v4, v10, v4, vcc
	v_cndmask_b32_e64 v10, v11, 6, vcc
	v_bitop3_b32 v11, v68, s30, v65 bitop3:0xc8
	v_cmp_eq_u32_e32 vcc, 0, v11
	v_cmp_gt_f32_e64 s[10:11], v5, v4
	s_and_b64 vcc, vcc, s[10:11]
	v_cndmask_b32_e32 v4, v4, v5, vcc
	v_cndmask_b32_e64 v5, v10, 7, vcc
	v_bitop3_b32 v10, v68, s31, v65 bitop3:0xc8
	v_cmp_eq_u32_e32 vcc, 0, v10
	v_cmp_gt_f32_e64 s[10:11], v14, v4
	s_and_b64 vcc, vcc, s[10:11]
	v_cndmask_b32_e32 v4, v4, v14, vcc
	v_bitop3_b32 v10, v68, s24, v65 bitop3:0xc8
	v_cndmask_b32_e64 v5, v5, 8, vcc
	v_cmp_eq_u32_e32 vcc, 0, v10
	v_cmp_gt_f32_e64 s[10:11], v15, v4
	s_and_b64 vcc, vcc, s[10:11]
	v_cndmask_b32_e32 v4, v4, v15, vcc
	v_bitop3_b32 v10, v68, s28, v65 bitop3:0xc8
	v_cndmask_b32_e64 v5, v5, 9, vcc
	v_cmp_eq_u32_e32 vcc, 0, v10
	v_cmp_gt_f32_e64 s[10:11], v44, v4
	s_and_b64 vcc, vcc, s[10:11]
; __device__ __forceinline__ void p8_route(Frame& F) {
;     ...
;             for (int s4 = 0; s4 < 4; ++s4) { float best = -INFINITY; int bi = 0;
;                 for (int e = 0; e < 32; ++e) { const float v = lr[e]; const bool ok = !((used >> e) & 1u) && (v > best); best = ok ? v : best; bi = ok ? e : bi; }
;                 used |= 1u << bi; idx[s4] = bi; val[s4] = best; }
;             const float e1 = __expf(val[1] - val[0]), e2 = __expf(val[2] - val[0]), e3 = __expf(val[3] - val[0]); const float inv = 1.f / (1.f + e1 + e2 + e3);
;             const float wv[4] = {inv, e1 * inv, e2 * inv, e3 * inv};
;             unsigned pos[4];
; #pragma unroll
;             for (int s4 = 0; s4 < 4; ++s4) pos[s4] = atomicAdd(F.ctl + CW_CNT + 64 * idx[s4], 1u);
; #pragma unroll
;             for (int s4 = 0; s4 < 4; ++s4) { RLIST[idx[s4] * ECAP + pos[s4]] = (m0 + tid) * 4 + s4; RWT[idx[s4] * ECAP + pos[s4]] = wv[s4]; } }
	v_cndmask_b32_e32 v4, v4, v44, vcc
	v_bitop3_b32 v10, v68, s33, v65 bitop3:0xc8
	v_cndmask_b32_e64 v5, v5, 10, vcc
	v_cmp_eq_u32_e32 vcc, 0, v10
	v_cmp_gt_f32_e64 s[10:11], v45, v4
	s_and_b64 vcc, vcc, s[10:11]
	v_cndmask_b32_e32 v4, v4, v45, vcc
	v_bitop3_b32 v10, v68, s34, v65 bitop3:0xc8
	v_cndmask_b32_e64 v5, v5, 11, vcc
	v_cmp_eq_u32_e32 vcc, 0, v10
	v_cmp_gt_f32_e64 s[10:11], v16, v4
	s_and_b64 vcc, vcc, s[10:11]
	v_cndmask_b32_e32 v4, v4, v16, vcc
	v_bitop3_b32 v10, v68, s35, v65 bitop3:0xc8
	v_cndmask_b32_e64 v5, v5, 12, vcc
	v_cmp_eq_u32_e32 vcc, 0, v10
	v_cmp_gt_f32_e64 s[10:11], v17, v4
	s_and_b64 vcc, vcc, s[10:11]
	v_cndmask_b32_e32 v4, v4, v17, vcc
	v_bitop3_b32 v10, v68, s36, v65 bitop3:0xc8
	v_cndmask_b32_e64 v5, v5, 13, vcc
	v_cmp_eq_u32_e32 vcc, 0, v10
	v_cmp_gt_f32_e64 s[10:11], v6, v4
	s_and_b64 vcc, vcc, s[10:11]
	v_cndmask_b32_e32 v4, v4, v6, vcc
	v_bitop3_b32 v6, v68, s37, v65 bitop3:0xc8
	v_cndmask_b32_e64 v5, v5, 14, vcc
	v_cmp_eq_u32_e32 vcc, 0, v6
	v_cmp_gt_f32_e64 s[10:11], v7, v4
	s_and_b64 vcc, vcc, s[10:11]
	v_cndmask_b32_e32 v4, v4, v7, vcc
	v_bitop3_b32 v6, v68, s38, v65 bitop3:0xc8
	v_cndmask_b32_e64 v5, v5, 15, vcc
	v_cmp_eq_u32_e32 vcc, 0, v6
	v_cmp_gt_f32_e64 s[10:11], v34, v4
	s_and_b64 vcc, vcc, s[10:11]
	v_cndmask_b32_e32 v4, v4, v34, vcc
	v_bitop3_b32 v6, v68, s39, v65 bitop3:0xc8
	v_cndmask_b32_e64 v5, v5, 16, vcc
	v_cmp_eq_u32_e32 vcc, 0, v6
	v_cmp_gt_f32_e64 s[10:11], v35, v4
	s_and_b64 vcc, vcc, s[10:11]
	v_cndmask_b32_e32 v4, v4, v35, vcc
	v_bitop3_b32 v6, v68, s40, v65 bitop3:0xc8
	v_cndmask_b32_e64 v5, v5, 17, vcc
	v_cmp_eq_u32_e32 vcc, 0, v6
	v_cmp_gt_f32_e64 s[10:11], v46, v4
	s_and_b64 vcc, vcc, s[10:11]
	v_cndmask_b32_e32 v4, v4, v46, vcc
	v_bitop3_b32 v6, v68, s41, v65 bitop3:0xc8
	v_cndmask_b32_e64 v5, v5, 18, vcc
	v_cmp_eq_u32_e32 vcc, 0, v6
	v_cmp_gt_f32_e64 s[10:11], v47, v4
	s_and_b64 vcc, vcc, s[10:11]
	v_cndmask_b32_e32 v4, v4, v47, vcc
	v_bitop3_b32 v6, v68, s42, v65 bitop3:0xc8
	v_cndmask_b32_e64 v5, v5, 19, vcc
	v_cmp_eq_u32_e32 vcc, 0, v6
	v_cmp_gt_f32_e64 s[10:11], v36, v4
	s_and_b64 vcc, vcc, s[10:11]
	v_cndmask_b32_e32 v4, v4, v36, vcc
	v_bitop3_b32 v6, v68, s43, v65 bitop3:0xc8
	v_cndmask_b32_e64 v5, v5, 20, vcc
	v_cmp_eq_u32_e32 vcc, 0, v6
	v_cmp_gt_f32_e64 s[10:11], v37, v4
	s_and_b64 vcc, vcc, s[10:11]
	v_cndmask_b32_e32 v4, v4, v37, vcc
	v_bitop3_b32 v6, v68, s44, v65 bitop3:0xc8
	v_cndmask_b32_e64 v5, v5, 21, vcc
	v_cmp_eq_u32_e32 vcc, 0, v6
	v_cmp_gt_f32_e64 s[10:11], v8, v4
	s_and_b64 vcc, vcc, s[10:11]
	v_cndmask_b32_e32 v4, v4, v8, vcc
	v_bitop3_b32 v6, v68, s45, v65 bitop3:0xc8
	v_cndmask_b32_e64 v5, v5, 22, vcc
	v_cmp_eq_u32_e32 vcc, 0, v6
	v_cmp_gt_f32_e64 s[10:11], v9, v4
	s_and_b64 vcc, vcc, s[10:11]
	v_cndmask_b32_e32 v4, v4, v9, vcc
	v_bitop3_b32 v6, v68, s46, v65 bitop3:0xc8
	v_cndmask_b32_e64 v5, v5, 23, vcc
	v_cmp_eq_u32_e32 vcc, 0, v6
	v_cmp_gt_f32_e64 s[10:11], v38, v4
	s_and_b64 vcc, vcc, s[10:11]
	v_cndmask_b32_e32 v4, v4, v38, vcc
	v_bitop3_b32 v6, v68, s47, v65 bitop3:0xc8
	v_cndmask_b32_e64 v5, v5, 24, vcc
	v_cmp_eq_u32_e32 vcc, 0, v6
	v_cmp_gt_f32_e64 s[10:11], v39, v4
	s_and_b64 vcc, vcc, s[10:11]
	v_cndmask_b32_e32 v4, v4, v39, vcc
	v_bitop3_b32 v6, v68, s48, v65 bitop3:0xc8
	v_cndmask_b32_e64 v5, v5, 25, vcc
	v_cmp_eq_u32_e32 vcc, 0, v6
	v_cmp_gt_f32_e64 s[10:11], v48, v4
	s_and_b64 vcc, vcc, s[10:11]
	v_cndmask_b32_e32 v4, v4, v48, vcc
	v_bitop3_b32 v6, v68, s49, v65 bitop3:0xc8
	v_cndmask_b32_e64 v5, v5, 26, vcc
	v_cmp_eq_u32_e32 vcc, 0, v6
	v_cmp_gt_f32_e64 s[10:11], v49, v4
	s_and_b64 vcc, vcc, s[10:11]
	v_cndmask_b32_e32 v4, v4, v49, vcc
	v_bitop3_b32 v6, v68, s50, v65 bitop3:0xc8
	v_cndmask_b32_e64 v5, v5, 27, vcc
	v_cmp_eq_u32_e32 vcc, 0, v6
	v_cmp_gt_f32_e64 s[10:11], v42, v4
	s_and_b64 vcc, vcc, s[10:11]
	v_cndmask_b32_e32 v4, v4, v42, vcc
	v_cndmask_b32_e64 v6, v5, 28, vcc
	v_bitop3_b32 v5, v68, s51, v65 bitop3:0xc8
	v_cmp_eq_u32_e32 vcc, 0, v5
	v_cmp_gt_f32_e64 s[10:11], v43, v4
	s_and_b64 vcc, vcc, s[10:11]
	v_lshlrev_b32_e32 v18, 6, v29
	v_cndmask_b32_e32 v7, v4, v43, vcc
	v_lshl_add_u64 v[4:5], v[18:19], 2, s[16:17]
	global_atomic_add v8, v[4:5], v60, off sc0
	v_bitop3_b32 v4, v68, 2.0, v65 bitop3:0xc8
	v_cndmask_b32_e64 v6, v6, 29, vcc
	v_cmp_eq_u32_e32 vcc, 0, v4
	v_cmp_gt_f32_e64 s[10:11], v2, v7
	s_and_b64 vcc, vcc, s[10:11]
	v_or_b32_e32 v69, v68, v65
	v_lshlrev_b32_e32 v18, 6, v64
	v_cndmask_b32_e32 v2, v7, v2, vcc
	v_lshl_add_u64 v[4:5], v[18:19], 2, s[16:17]
	v_cndmask_b32_e64 v6, v6, 30, vcc
	v_cmp_lt_i32_e32 vcc, -1, v69
	v_cmp_gt_f32_e64 s[10:11], v3, v2
	global_atomic_add v9, v[4:5], v60, off sc0
	v_lshlrev_b32_e32 v18, 6, v66
	s_and_b64 vcc, vcc, s[10:11]
	v_lshl_add_u64 v[4:5], v[18:19], 2, s[16:17]
	v_cndmask_b32_e64 v6, v6, 31, vcc
	global_atomic_add v7, v[4:5], v60, off sc0
	v_lshlrev_b32_e32 v18, 6, v6
	v_cndmask_b32_e32 v4, v2, v3, vcc
	v_lshl_add_u64 v[2:3], v[18:19], 2, s[16:17]
	global_atomic_add v10, v[2:3], v60, off sc0
	v_sub_f32_e32 v2, v63, v62
	v_mul_f32_e32 v2, 0x3fb8aa3b, v2
	v_sub_f32_e32 v3, v67, v62
	v_exp_f32_e32 v2, v2
	v_mul_f32_e32 v3, 0x3fb8aa3b, v3
	v_sub_f32_e32 v4, v4, v62
	v_exp_f32_e32 v3, v3
	v_mul_f32_e32 v4, 0x3fb8aa3b, v4
	v_exp_f32_e32 v4, v4
	v_add_f32_e32 v5, 1.0, v2
	v_add_f32_e32 v5, v5, v3
	v_add_f32_e32 v5, v5, v4
	v_div_scale_f32 v11, s[10:11], v5, v5, 1.0
	v_rcp_f32_e32 v12, v11
	s_waitcnt vmcnt(3)
	v_lshl_add_u32 v18, v29, 14, v8
	v_fma_f32 v13, -v11, v12, 1.0
	v_fmac_f32_e32 v12, v13, v12
	v_div_scale_f32 v13, vcc, 1.0, v5, 1.0
	v_mul_f32_e32 v14, v13, v12
	v_fma_f32 v15, -v11, v14, v13
	v_fmac_f32_e32 v14, v15, v12
	v_fma_f32 v11, -v11, v14, v13
	v_div_fmas_f32 v11, v11, v12, v14
	v_div_fixup_f32 v11, v11, v5, 1.0
	v_mul_f32_e32 v12, v2, v11
	v_mul_f32_e32 v13, v3, v11
	v_lshlrev_b64 v[2:3], 2, v[18:19]
	v_mul_f32_e32 v14, v4, v11
	v_lshl_add_u64 v[4:5], s[2:3], 0, v[2:3]
	v_lshl_add_u64 v[2:3], s[14:15], 0, v[2:3]
	s_waitcnt vmcnt(2)
	v_lshl_add_u32 v18, v64, 14, v9
	v_lshl_or_b32 v15, s52, 7, v163
	global_store_dword v[2:3], v11, off
	v_lshlrev_b64 v[2:3], 2, v[18:19]
	global_store_dword v[4:5], v15, off
	v_lshl_add_u64 v[4:5], s[2:3], 0, v[2:3]
	v_lshl_add_u64 v[2:3], s[14:15], 0, v[2:3]
	s_waitcnt vmcnt(3)
	v_lshl_add_u32 v18, v66, 14, v7
	v_or_b32_e32 v8, 1, v15
	global_store_dword v[2:3], v12, off
	v_lshlrev_b64 v[2:3], 2, v[18:19]
	global_store_dword v[4:5], v8, off
	v_lshl_add_u64 v[4:5], s[2:3], 0, v[2:3]
	v_lshl_add_u64 v[2:3], s[14:15], 0, v[2:3]
	s_waitcnt vmcnt(4)
	v_lshl_add_u32 v18, v6, 14, v10
	v_or_b32_e32 v8, 2, v15
	global_store_dword v[2:3], v13, off
	v_lshlrev_b64 v[2:3], 2, v[18:19]
	global_store_dword v[4:5], v8, off
	v_or_b32_e32 v7, 3, v15
	v_lshl_add_u64 v[4:5], s[2:3], 0, v[2:3]
	v_lshl_add_u64 v[2:3], s[14:15], 0, v[2:3]
	global_store_dword v[4:5], v7, off
	global_store_dword v[2:3], v14, off
	s_branch .LBB0_1425
